# gMLP row-statistics loop: next iteration's four loads requested before this iteration's gelu work (register double buffer)
# baseline (speedup 1.0000x reference)
; #define LAS __attribute__((address_space(3)))
; __device__ __forceinline__ float bflo(unsigned w) { return __uint_as_float(w << 16); }
; __device__ __forceinline__ float bfhi(unsigned w) { return __uint_as_float(w & 0xffff0000u); }
; __device__ __forceinline__ float gelu_fast(float x) { const float y = 1.5957691216057308f * (x + 0.044715f * x * x * x); return x * __builtin_amdgcn_rcpf(1.f + __expf(-y)); }
; __device__ __forceinline__ void gmlp_fast_unit(int ci, const bf16_t* P, const float* gnorm, const bf16_t* Wb, const float* bs_, bf16_t* AO, LAS unsigned char* lds) {
;     ...
;     __syncthreads();
;     *(LAS f32x2*)(gnl + 2 * tid) = *(const f32x2*)(gnorm + 2 * tid); *(LAS f32x2*)(bsl + 2 * tid) = *(const f32x2*)(bs_ + 2 * tid);
;     { const int row = tid >> 2, qq = tid & 3; const u32x4* vp = (const u32x4*)(P + (size_t)(row0 + row) * LDP0 + 3072 + qq * 256); float ss = 0.f;
; #pragma unroll 4
;         for (int i = 0; i < 32; ++i) { const u32x4 w = vp[i]; const unsigned ww[4] = {w.x, w.y, w.z, w.w};
; #pragma unroll
;             for (int c = 0; c < 4; ++c) { const float a0 = gelu_fast(bflo(ww[c])), a1 = gelu_fast(bfhi(ww[c])); ss += a0 * a0 + a1 * a1; } }
;         ss += __shfl_xor(ss, 1); ss += __shfl_xor(ss, 2);
;         if (qq == 0) rs[row] = rsqrtf(ss * (1.f / 1024.f) + EPS); }
.LBB0_287:
	s_and_b64 vcc, exec, s[2:3]
	s_cbranch_vccz .LBB0_274
	s_barrier
	global_load_dwordx2 v[4:5], v[132:133], off
	global_load_dwordx2 v[6:7], v[134:135], off
	s_lshl_b32 s2, s44, 7
	s_add_i32 s3, s2, 0x7fffc000
	s_and_b32 s8, s2, 0x80
	s_and_b32 s3, s3, 0x7fffff00
	s_or_b32 s3, s3, s8
	s_addk_i32 s3, 0x4000
	s_cmpk_lt_u32 s44, 0x80
	s_cselect_b32 s8, s2, s3
	v_or_b32_e32 v2, s8, v1
	v_mad_u64_u32 v[2:3], s[2:3], v2, s27, v[136:137]
	v_mov_b32_e32 v36, 0
	s_mov_b64 s[2:3], 0
	s_waitcnt vmcnt(0)
	ds_write2st64_b64 v129, v[4:5], v[6:7] offset0:80 offset1:88
	v_lshl_add_u64 v[198:199], v[2:3], 0, s[2:3]
	global_load_dwordx4 v[200:203], v[198:199], off offset:-32
	global_load_dwordx4 v[204:207], v[198:199], off offset:-16
	global_load_dwordx4 v[208:211], v[198:199], off
	global_load_dwordx4 v[212:215], v[198:199], off offset:16
.LBB0_289:
	s_waitcnt vmcnt(0)
	v_mov_b32_e32 v10, v200
	v_mov_b32_e32 v11, v201
	v_mov_b32_e32 v12, v202
	v_mov_b32_e32 v13, v203
	v_mov_b32_e32 v18, v204
	v_mov_b32_e32 v19, v205
	v_mov_b32_e32 v20, v206
	v_mov_b32_e32 v21, v207
	v_mov_b32_e32 v26, v208
	v_mov_b32_e32 v27, v209
	v_mov_b32_e32 v28, v210
	v_mov_b32_e32 v29, v211
	v_mov_b32_e32 v38, v212
	v_mov_b32_e32 v39, v213
	v_mov_b32_e32 v40, v214
	v_mov_b32_e32 v41, v215
	s_add_u32 s2, s2, 64
	s_addc_u32 s3, s3, 0
	v_lshl_add_u64 v[198:199], v[2:3], 0, s[2:3]
	global_load_dwordx4 v[200:203], v[198:199], off offset:-32
	global_load_dwordx4 v[204:207], v[198:199], off offset:-16
	global_load_dwordx4 v[208:211], v[198:199], off
	global_load_dwordx4 v[212:215], v[198:199], off offset:16
	s_cmpk_eq_i32 s2, 0x200
	v_lshlrev_b32_e32 v4, 16, v10
	v_and_b32_e32 v5, 0xffff0000, v10
	v_lshlrev_b32_e32 v7, 16, v12
	v_lshlrev_b32_e32 v6, 16, v11
	v_and_b32_e32 v9, 0xffff0000, v12
	v_and_b32_e32 v8, 0xffff0000, v11
	v_lshlrev_b32_e32 v10, 16, v13
	v_and_b32_e32 v11, 0xffff0000, v13
	v_lshlrev_b32_e32 v12, 16, v18
	v_and_b32_e32 v13, 0xffff0000, v18
	v_lshlrev_b32_e32 v14, 16, v19
	v_and_b32_e32 v16, 0xffff0000, v19
	v_lshlrev_b32_e32 v18, 16, v21
	v_and_b32_e32 v19, 0xffff0000, v21
	v_lshlrev_b32_e32 v30, 16, v39
	v_and_b32_e32 v32, 0xffff0000, v39
	v_mul_f32_e32 v37, 0x3d372713, v4
	v_mul_f32_e32 v39, 0x3d372713, v5
	v_lshlrev_b32_e32 v15, 16, v20
	v_and_b32_e32 v17, 0xffff0000, v20
	v_lshlrev_b32_e32 v20, 16, v26
	v_and_b32_e32 v21, 0xffff0000, v26
	v_lshlrev_b32_e32 v23, 16, v28
	v_lshlrev_b32_e32 v22, 16, v27
	v_and_b32_e32 v25, 0xffff0000, v28
	v_and_b32_e32 v24, 0xffff0000, v27
	v_lshlrev_b32_e32 v26, 16, v29
	v_and_b32_e32 v27, 0xffff0000, v29
	v_lshlrev_b32_e32 v28, 16, v38
	v_and_b32_e32 v29, 0xffff0000, v38
	v_lshlrev_b32_e32 v31, 16, v40
	v_and_b32_e32 v33, 0xffff0000, v40
	v_lshlrev_b32_e32 v34, 16, v41
	v_and_b32_e32 v35, 0xffff0000, v41
	v_mov_b32_e32 v38, v4
	v_mov_b32_e32 v40, v5
	v_mul_f32_e32 v41, 0x3d372713, v6
	v_mul_f32_e32 v43, 0x3d372713, v8
	v_mul_f32_e32 v45, 0x3d372713, v7
	v_mul_f32_e32 v47, 0x3d372713, v9
	v_mul_f32_e32 v51, 0x3d372713, v11
	v_mul_f32_e32 v53, 0x3d372713, v12
	v_mul_f32_e32 v55, 0x3d372713, v13
	v_mul_f32_e32 v65, 0x3d372713, v18
	v_mul_f32_e32 v67, 0x3d372713, v19
	v_mul_f32_e32 v37, v37, v4
	v_mul_f32_e32 v39, v39, v5
	v_mov_b32_e32 v42, v6
	v_mov_b32_e32 v44, v8
	v_mov_b32_e32 v46, v7
	v_mov_b32_e32 v48, v9
	v_mul_f32_e32 v49, 0x3d372713, v10
	v_mov_b32_e32 v52, v11
	v_mov_b32_e32 v54, v12
	v_mov_b32_e32 v56, v13
	v_mul_f32_e32 v57, 0x3d372713, v14
	v_mov_b32_e32 v66, v18
	v_mov_b32_e32 v68, v19
	v_mul_f32_e32 v69, 0x3d372713, v20
	v_mul_f32_e32 v41, v41, v6
	v_mul_f32_e32 v43, v43, v8
	v_mul_f32_e32 v45, v45, v7
	v_mul_f32_e32 v47, v47, v9
	v_mul_f32_e32 v51, v51, v11
	v_mul_f32_e32 v53, v53, v12
	v_mul_f32_e32 v55, v55, v13
	v_mul_f32_e32 v65, v65, v18
	v_mul_f32_e32 v67, v67, v19
	v_fmac_f32_e32 v38, v37, v38
	v_fmac_f32_e32 v40, v39, v40
	v_mov_b32_e32 v50, v10
	v_mov_b32_e32 v58, v14
	v_mov_b32_e32 v70, v20
	v_mul_f32_e32 v49, v49, v10
	v_mul_f32_e32 v57, v57, v14
	v_mul_f32_e32 v69, v69, v20
	v_fmac_f32_e32 v42, v41, v42
	v_fmac_f32_e32 v44, v43, v44
	v_fmac_f32_e32 v46, v45, v46
	v_fmac_f32_e32 v48, v47, v48
	v_fmac_f32_e32 v52, v51, v52
	v_fmac_f32_e32 v54, v53, v54
	v_fmac_f32_e32 v56, v55, v56
	v_fmac_f32_e32 v66, v65, v66
	v_fmac_f32_e32 v68, v67, v68
	v_mul_f32_e32 v37, 0xbfcc422a, v38
	v_mul_f32_e32 v38, 0xbfcc422a, v40
	v_fmac_f32_e32 v50, v49, v50
	v_fmac_f32_e32 v58, v57, v58
	v_fmac_f32_e32 v70, v69, v70
	v_mul_f32_e32 v39, 0xbfcc422a, v42
	v_mul_f32_e32 v40, 0xbfcc422a, v44
	v_mul_f32_e32 v41, 0xbfcc422a, v46
	v_mul_f32_e32 v42, 0xbfcc422a, v48
	v_mul_f32_e32 v44, 0xbfcc422a, v52
	v_mul_f32_e32 v45, 0xbfcc422a, v54
	v_mul_f32_e32 v46, 0xbfcc422a, v56
	v_mul_f32_e32 v51, 0xbfcc422a, v66
	v_mul_f32_e32 v52, 0xbfcc422a, v68
	v_mul_f32_e32 v37, 0x3fb8aa3b, v37
	v_mul_f32_e32 v38, 0x3fb8aa3b, v38
	v_mul_f32_e32 v59, 0x3d372713, v16
	v_mul_f32_e32 v63, 0x3d372713, v17
	v_mul_f32_e32 v43, 0xbfcc422a, v50
	v_mul_f32_e32 v47, 0xbfcc422a, v58
	v_mul_f32_e32 v53, 0xbfcc422a, v70
	v_mul_f32_e32 v39, 0x3fb8aa3b, v39
	v_mul_f32_e32 v40, 0x3fb8aa3b, v40
	v_mul_f32_e32 v42, 0x3fb8aa3b, v42
	v_mul_f32_e32 v45, 0x3fb8aa3b, v45
	v_mul_f32_e32 v46, 0x3fb8aa3b, v46
	v_mul_f32_e32 v51, 0x3fb8aa3b, v51
	v_mul_f32_e32 v52, 0x3fb8aa3b, v52
	v_exp_f32_e32 v37, v37
	v_exp_f32_e32 v38, v38
	v_mov_b32_e32 v60, v16
	v_mul_f32_e32 v61, 0x3d372713, v15
	v_mov_b32_e32 v64, v17
	v_mul_f32_e32 v59, v59, v16
	v_mul_f32_e32 v63, v63, v17
	v_mul_f32_e32 v41, 0x3fb8aa3b, v41
	v_mul_f32_e32 v43, 0x3fb8aa3b, v43
	v_mul_f32_e32 v47, 0x3fb8aa3b, v47
	v_mul_f32_e32 v53, 0x3fb8aa3b, v53
	v_exp_f32_e32 v39, v39
	v_exp_f32_e32 v40, v40
; __device__ __forceinline__ float bflo(unsigned w) { return __uint_as_float(w << 16); }
; __device__ __forceinline__ float bfhi(unsigned w) { return __uint_as_float(w & 0xffff0000u); }
; __device__ __forceinline__ float gelu_fast(float x) { const float y = 1.5957691216057308f * (x + 0.044715f * x * x * x); return x * __builtin_amdgcn_rcpf(1.f + __expf(-y)); }
; __device__ __forceinline__ void gmlp_fast_unit(int ci, const bf16_t* P, const float* gnorm, const bf16_t* Wb, const float* bs_, bf16_t* AO, LAS unsigned char* lds) {
;     ...
;         for (int i = 0; i < 32; ++i) { const u32x4 w = vp[i]; const unsigned ww[4] = {w.x, w.y, w.z, w.w};
; #pragma unroll
;             for (int c = 0; c < 4; ++c) { const float a0 = gelu_fast(bflo(ww[c])), a1 = gelu_fast(bfhi(ww[c])); ss += a0 * a0 + a1 * a1; } }
	v_exp_f32_e32 v42, v42
	v_exp_f32_e32 v45, v45
	v_exp_f32_e32 v46, v46
	v_exp_f32_e32 v51, v51
	v_exp_f32_e32 v52, v52
	v_mov_b32_e32 v62, v15
	v_mul_f32_e32 v71, 0x3d372713, v21
	v_mul_f32_e32 v75, 0x3d372713, v24
	v_mul_f32_e32 v79, 0x3d372713, v25
	v_mul_f32_e32 v61, v61, v15
	v_fmac_f32_e32 v60, v59, v60
	v_fmac_f32_e32 v64, v63, v64
	v_mul_f32_e32 v44, 0x3fb8aa3b, v44
	v_exp_f32_e32 v41, v41
	v_exp_f32_e32 v43, v43
	v_exp_f32_e32 v47, v47
	v_exp_f32_e32 v53, v53
	v_mov_b32_e32 v72, v21
	v_mov_b32_e32 v76, v24
	v_mov_b32_e32 v80, v25
	v_mul_f32_e32 v81, 0x3d372713, v26
	v_mul_f32_e32 v71, v71, v21
	v_mul_f32_e32 v75, v75, v24
	v_mul_f32_e32 v79, v79, v25
	v_fmac_f32_e32 v62, v61, v62
	v_mul_f32_e32 v48, 0xbfcc422a, v60
	v_mul_f32_e32 v50, 0xbfcc422a, v64
	v_exp_f32_e32 v44, v44
	v_mul_f32_e32 v73, 0x3d372713, v22
	v_mul_f32_e32 v77, 0x3d372713, v23
	v_mov_b32_e32 v82, v26
	v_mul_f32_e32 v81, v81, v26
	v_fmac_f32_e32 v72, v71, v72
	v_fmac_f32_e32 v76, v75, v76
	v_fmac_f32_e32 v80, v79, v80
	v_mul_f32_e32 v49, 0xbfcc422a, v62
	v_mul_f32_e32 v48, 0x3fb8aa3b, v48
	v_mul_f32_e32 v50, 0x3fb8aa3b, v50
	v_add_f32_e32 v37, 1.0, v37
	v_add_f32_e32 v69, 1.0, v38
	v_mov_b32_e32 v74, v22
	v_mov_b32_e32 v78, v23
	v_mul_f32_e32 v73, v73, v22
	v_mul_f32_e32 v77, v77, v23
	v_fmac_f32_e32 v82, v81, v82
	v_mul_f32_e32 v54, 0xbfcc422a, v72
	v_mul_f32_e32 v56, 0xbfcc422a, v76
	v_mul_f32_e32 v58, 0xbfcc422a, v80
	v_mul_f32_e32 v49, 0x3fb8aa3b, v49
	v_exp_f32_e32 v48, v48
	v_exp_f32_e32 v50, v50
	v_add_f32_e32 v70, 1.0, v39
	v_add_f32_e32 v71, 1.0, v40
	v_add_f32_e32 v72, 1.0, v42
	v_add_f32_e32 v75, 1.0, v45
	v_add_f32_e32 v76, 1.0, v46
	v_add_f32_e32 v80, 1.0, v51
	v_add_f32_e32 v81, 1.0, v52
	v_rcp_f32_e32 v38, v37
	v_rcp_f32_e32 v39, v69
	v_mul_f32_e32 v83, 0x3d372713, v27
	v_fmac_f32_e32 v74, v73, v74
	v_fmac_f32_e32 v78, v77, v78
	v_mul_f32_e32 v59, 0xbfcc422a, v82
	v_exp_f32_e32 v49, v49
	v_add_f32_e32 v41, 1.0, v41
	v_add_f32_e32 v73, 1.0, v43
	v_add_f32_e32 v77, 1.0, v47
	v_add_f32_e32 v82, 1.0, v53
	v_rcp_f32_e32 v42, v71
	v_rcp_f32_e32 v43, v72
	v_rcp_f32_e32 v46, v75
	v_rcp_f32_e32 v47, v76
	v_rcp_f32_e32 v52, v80
	v_rcp_f32_e32 v53, v81
	v_mov_b32_e32 v84, v27
	v_mul_f32_e32 v85, 0x3d372713, v28
	v_mul_f32_e32 v87, 0x3d372713, v29
	v_mul_f32_e32 v83, v83, v27
	v_mul_f32_e32 v55, 0xbfcc422a, v74
	v_mul_f32_e32 v54, 0x3fb8aa3b, v54
	v_add_f32_e32 v74, 1.0, v44
	v_rcp_f32_e32 v40, v70
	v_rcp_f32_e32 v41, v41
	v_mov_b32_e32 v86, v28
	v_mov_b32_e32 v88, v29
	v_mul_f32_e32 v89, 0x3d372713, v30
	v_mul_f32_e32 v91, 0x3d372713, v32
	v_mul_f32_e32 v95, 0x3d372713, v33
	v_mul_f32_e32 v85, v85, v28
	v_mul_f32_e32 v87, v87, v29
	v_fmac_f32_e32 v84, v83, v84
	v_mul_f32_e32 v57, 0xbfcc422a, v78
	v_mul_f32_e32 v55, 0x3fb8aa3b, v55
	v_mul_f32_e32 v56, 0x3fb8aa3b, v56
	v_mul_f32_e32 v58, 0x3fb8aa3b, v58
	v_exp_f32_e32 v54, v54
	v_rcp_f32_e32 v44, v73
	v_rcp_f32_e32 v45, v74
	v_mov_b32_e32 v90, v30
	v_mov_b32_e32 v92, v32
	v_mul_f32_e32 v93, 0x3d372713, v31
	v_mov_b32_e32 v96, v33
	v_mul_f32_e32 v97, 0x3d372713, v34
	v_mul_f32_e32 v89, v89, v30
	v_mul_f32_e32 v91, v91, v32
	v_mul_f32_e32 v95, v95, v33
	v_fmac_f32_e32 v86, v85, v86
	v_fmac_f32_e32 v88, v87, v88
	v_mul_f32_e32 v60, 0xbfcc422a, v84
	v_mul_f32_e32 v57, 0x3fb8aa3b, v57
	v_mul_f32_e32 v59, 0x3fb8aa3b, v59
	v_exp_f32_e32 v55, v55
	v_exp_f32_e32 v56, v56
	v_exp_f32_e32 v58, v58
	v_add_f32_e32 v78, 1.0, v48
	v_add_f32_e32 v79, 1.0, v50
	v_pk_mul_f32 v[4:5], v[38:39], v[4:5]
	v_mov_b32_e32 v94, v31
	v_mov_b32_e32 v98, v34
	v_mul_f32_e32 v99, 0x3d372713, v35
	v_mul_f32_e32 v93, v93, v31
	v_mul_f32_e32 v97, v97, v34
	v_fmac_f32_e32 v90, v89, v90
	v_fmac_f32_e32 v92, v91, v92
	v_fmac_f32_e32 v96, v95, v96
	v_mul_f32_e32 v61, 0xbfcc422a, v86
	v_mul_f32_e32 v62, 0xbfcc422a, v88
	v_mul_f32_e32 v60, 0x3fb8aa3b, v60
	v_exp_f32_e32 v57, v57
	v_exp_f32_e32 v59, v59
	v_add_f32_e32 v49, 1.0, v49
	v_rcp_f32_e32 v50, v78
	v_rcp_f32_e32 v51, v79
	v_pk_mul_f32 v[8:9], v[42:43], v[8:9]
	v_pk_mul_f32 v[12:13], v[46:47], v[12:13]
	v_pk_mul_f32 v[18:19], v[52:53], v[18:19]
	v_pk_mul_f32 v[4:5], v[4:5], v[4:5]
	v_mov_b32_e32 v100, v35
	v_mul_f32_e32 v99, v99, v35
	v_fmac_f32_e32 v94, v93, v94
	v_fmac_f32_e32 v98, v97, v98
	v_mul_f32_e32 v63, 0xbfcc422a, v90
	v_mul_f32_e32 v64, 0xbfcc422a, v92
; __device__ __forceinline__ float bflo(unsigned w) { return __uint_as_float(w << 16); }
; __device__ __forceinline__ float bfhi(unsigned w) { return __uint_as_float(w & 0xffff0000u); }
; __device__ __forceinline__ float gelu_fast(float x) { const float y = 1.5957691216057308f * (x + 0.044715f * x * x * x); return x * __builtin_amdgcn_rcpf(1.f + __expf(-y)); }
; __device__ __forceinline__ void gmlp_fast_unit(int ci, const bf16_t* P, const float* gnorm, const bf16_t* Wb, const float* bs_, bf16_t* AO, LAS unsigned char* lds) {
;     ...
;         for (int i = 0; i < 32; ++i) { const u32x4 w = vp[i]; const unsigned ww[4] = {w.x, w.y, w.z, w.w};
; #pragma unroll
;             for (int c = 0; c < 4; ++c) { const float a0 = gelu_fast(bflo(ww[c])), a1 = gelu_fast(bfhi(ww[c])); ss += a0 * a0 + a1 * a1; } }
;         ss += __shfl_xor(ss, 1); ss += __shfl_xor(ss, 2);
;         if (qq == 0) rs[row] = rsqrtf(ss * (1.f / 1024.f) + EPS); }
	v_mul_f32_e32 v66, 0xbfcc422a, v96
	v_mul_f32_e32 v61, 0x3fb8aa3b, v61
	v_mul_f32_e32 v62, 0x3fb8aa3b, v62
	v_exp_f32_e32 v60, v60
	v_rcp_f32_e32 v48, v77
	v_rcp_f32_e32 v49, v49
	v_pk_mul_f32 v[6:7], v[40:41], v[6:7]
	v_pk_mul_f32 v[8:9], v[8:9], v[8:9]
	v_pk_mul_f32 v[12:13], v[12:13], v[12:13]
	v_pk_mul_f32 v[18:19], v[18:19], v[18:19]
	v_add_f32_e32 v37, v4, v5
	v_fmac_f32_e32 v100, v99, v100
	v_mul_f32_e32 v65, 0xbfcc422a, v94
	v_mul_f32_e32 v67, 0xbfcc422a, v98
	v_mul_f32_e32 v63, 0x3fb8aa3b, v63
	v_mul_f32_e32 v64, 0x3fb8aa3b, v64
	v_mul_f32_e32 v66, 0x3fb8aa3b, v66
	v_exp_f32_e32 v61, v61
	v_exp_f32_e32 v62, v62
	v_add_f32_e32 v83, 1.0, v54
	v_pk_mul_f32 v[10:11], v[44:45], v[10:11]
	v_pk_fma_f32 v[4:5], v[6:7], v[6:7], v[8:9]
	v_add_f32_e32 v12, v12, v13
	v_add_f32_e32 v13, v18, v19
	v_add_f32_e32 v18, v36, v37
	v_mul_f32_e32 v68, 0xbfcc422a, v100
	v_mul_f32_e32 v65, 0x3fb8aa3b, v65
	v_mul_f32_e32 v67, 0x3fb8aa3b, v67
	v_exp_f32_e32 v63, v63
	v_exp_f32_e32 v64, v64
	v_exp_f32_e32 v66, v66
	v_add_f32_e32 v84, 1.0, v55
	v_add_f32_e32 v85, 1.0, v56
	v_add_f32_e32 v86, 1.0, v58
	v_rcp_f32_e32 v54, v82
	v_rcp_f32_e32 v55, v83
	v_pk_mul_f32 v[10:11], v[10:11], v[10:11]
	v_add_f32_e32 v4, v4, v18
	v_mul_f32_e32 v68, 0x3fb8aa3b, v68
	v_exp_f32_e32 v65, v65
	v_exp_f32_e32 v67, v67
	v_add_f32_e32 v57, 1.0, v57
	v_add_f32_e32 v87, 1.0, v59
	v_rcp_f32_e32 v58, v85
	v_rcp_f32_e32 v59, v86
	v_pk_mul_f32 v[16:17], v[50:51], v[16:17]
	v_add_f32_e32 v38, v10, v11
	v_add_f32_e32 v4, v5, v4
	v_exp_f32_e32 v68, v68
	v_add_f32_e32 v88, 1.0, v60
	v_rcp_f32_e32 v56, v84
	v_rcp_f32_e32 v57, v57
	v_pk_mul_f32 v[14:15], v[48:49], v[14:15]
	v_pk_mul_f32 v[16:17], v[16:17], v[16:17]
	v_add_f32_e32 v4, v38, v4
	v_add_f32_e32 v89, 1.0, v61
	v_add_f32_e32 v90, 1.0, v62
	v_rcp_f32_e32 v60, v87
	v_rcp_f32_e32 v61, v88
	v_pk_fma_f32 v[6:7], v[14:15], v[14:15], v[16:17]
	v_add_f32_e32 v4, v4, v12
	v_add_f32_e32 v91, 1.0, v63
	v_add_f32_e32 v92, 1.0, v64
	v_add_f32_e32 v93, 1.0, v66
	v_rcp_f32_e32 v62, v89
	v_rcp_f32_e32 v63, v90
	v_pk_mul_f32 v[20:21], v[54:55], v[20:21]
	v_add_f32_e32 v4, v6, v4
	v_add_f32_e32 v65, 1.0, v65
	v_add_f32_e32 v94, 1.0, v67
	v_rcp_f32_e32 v66, v92
	v_rcp_f32_e32 v67, v93
	v_pk_mul_f32 v[24:25], v[58:59], v[24:25]
	v_pk_mul_f32 v[20:21], v[20:21], v[20:21]
	v_add_f32_e32 v4, v7, v4
	v_add_f32_e32 v95, 1.0, v68
	v_rcp_f32_e32 v64, v91
	v_rcp_f32_e32 v65, v65
	v_pk_mul_f32 v[22:23], v[56:57], v[22:23]
	v_pk_mul_f32 v[24:25], v[24:25], v[24:25]
	v_add_f32_e32 v14, v20, v21
	v_add_f32_e32 v4, v13, v4
	v_rcp_f32_e32 v68, v94
	v_rcp_f32_e32 v69, v95
	v_pk_mul_f32 v[26:27], v[60:61], v[26:27]
	v_pk_fma_f32 v[8:9], v[22:23], v[22:23], v[24:25]
	v_add_f32_e32 v4, v4, v14
	v_pk_mul_f32 v[28:29], v[62:63], v[28:29]
	v_pk_mul_f32 v[26:27], v[26:27], v[26:27]
	v_add_f32_e32 v4, v8, v4
	v_pk_mul_f32 v[32:33], v[66:67], v[32:33]
	v_pk_mul_f32 v[28:29], v[28:29], v[28:29]
	v_add_f32_e32 v15, v26, v27
	v_add_f32_e32 v4, v9, v4
	v_pk_mul_f32 v[30:31], v[64:65], v[30:31]
	v_pk_mul_f32 v[32:33], v[32:33], v[32:33]
	v_add_f32_e32 v16, v28, v29
	v_add_f32_e32 v4, v15, v4
	v_pk_mul_f32 v[34:35], v[68:69], v[34:35]
	v_pk_fma_f32 v[10:11], v[30:31], v[30:31], v[32:33]
	v_add_f32_e32 v4, v4, v16
	v_pk_mul_f32 v[34:35], v[34:35], v[34:35]
	v_add_f32_e32 v4, v10, v4
	v_add_f32_e32 v17, v34, v35
	v_add_f32_e32 v4, v11, v4
	v_add_f32_e32 v36, v17, v4
	s_cbranch_scc0 .LBB0_289
	v_and_b32_e32 v3, 64, v196
	v_xor_b32_e32 v2, 1, v196
	v_add_u32_e32 v3, 64, v3
	v_cmp_lt_i32_e32 vcc, v2, v3
	v_xor_b32_e32 v4, 2, v196
	v_readfirstlane_b32 s9, v0
	v_cndmask_b32_e32 v2, v196, v2, vcc
	v_lshlrev_b32_e32 v2, 2, v2
	ds_bpermute_b32 v2, v2, v36
	v_cmp_lt_i32_e32 vcc, v4, v3
	s_waitcnt lgkmcnt(0)
	v_add_f32_e32 v2, v36, v2
	v_cndmask_b32_e32 v3, v196, v4, vcc
	v_lshlrev_b32_e32 v3, 2, v3
	ds_bpermute_b32 v3, v3, v2
	s_and_saveexec_b64 s[2:3], s[6:7]
	s_cbranch_execz .LBB0_292
	s_waitcnt lgkmcnt(0)
	v_add_f32_e32 v2, v2, v3
	v_fmamk_f32 v2, v2, 0x3a800000, v188
	s_mov_b32 s14, 0x800000
	v_mul_f32_e32 v3, 0x4b800000, v2
	v_cmp_gt_f32_e32 vcc, s14, v2
	s_nop 1
	v_cndmask_b32_e32 v2, v2, v3, vcc
	v_rsq_f32_e32 v2, v2
	s_nop 0
	v_mul_f32_e32 v3, 0x45800000, v2
	v_cndmask_b32_e32 v2, v2, v3, vcc
	ds_write_b32 v177, v2 offset:36864
